# loop-edge edit: first ds_reads of the K-loop issued before the pointer-update SALU chain (MoE up and down), on top of v_mov_b64 init
# speedup vs baseline: 1.0020x; 1.0020x over previous
; #define PG8_STAGE(bufoff, gbase, voff) do { _Pragma("unroll") for (int _i = 0; _i < 2; ++_i) \
;         __builtin_amdgcn_global_load_lds((const unsigned*)((const char*)(gbase) + (voff)[_i]), (PG8_LAS unsigned*)(lds + (bufoff) + ldsw + _i * 8192), 16, 0, 0); } while (0)
; #define PG8_STAGE_G(bufoff, kb, g) do { _Pragma("unroll") for (int _i = 0; _i < 2; ++_i) \
;         __builtin_amdgcn_global_load_lds((const unsigned*)(gA + (size_t)(kb) + (g)[_i]), (PG8_LAS unsigned*)(lds + (bufoff) + ldsw + _i * 8192), 16, 0, 0); } while (0)
; #define PG8_WAIT_V(n) asm volatile("s_waitcnt vmcnt(" #n ")" ::: "memory")
; #define PG8_WAIT_L(n) asm volatile("s_waitcnt lgkmcnt(" #n ")" ::: "memory")
; #define PG8_BAR __builtin_amdgcn_s_barrier()
; template <class Epi, class Sched, bool ALIGN_EPI = false, bool SP2 = false, bool GATHER = false, bool HALFM = false>
; __device__ __forceinline__ void gemm_phase(PG8_LAS unsigned char* lds, const int Kdim, const Sched& S, const Epi& E) {
;     ...
;             const bool last = (t == nt - 2);
;             const char* a1 = cA + (size_t)(t + 1) * kstep;
;             const char* a2 = last ? nA : cA + (size_t)(t + 2) * kstep; const char* b2 = last ? nB : cB + (size_t)(t + 2) * kstep;
;             const char* a3 = a2 + kstep; const char* b3 = b2 + kstep;
;             if (last && has_next) S.a_ready(nxt);
;             unsigned s0[2] = {0u, 0u}, s1[2] = {0u, 0u}; size_t kb2 = 0;
;             if constexpr (GATHER) { kb2 = last ? (size_t)0 : (size_t)(t + 2) * kstep;
; #pragma unroll
;                 for (int i = 0; i < 2; ++i) { s0[i] = last ? gn[0][i] : gc[0][i]; s1[i] = last ? gn[1][i] : gc[1][i]; } }
;             if constexpr (SP2) {
;             PG8_LDB(B0, 0, 0); PG8_LDB(B1, 0, 1); PG8_SCHED; PG8_LDA(At, 0, 0); if constexpr (GATHER) PG8_STAGE_G(PG8_SA(1, 1), (size_t)(t + 1) * kstep, gc[1]); else PG8_STAGE(PG8_SA(1, 1), a1 + hstep, voffA);
;             PG8_WAIT_V(8); PG8_WAIT_L(0); PG8_BAR; PG8_MMA(0, 0, At, B0); PG8_MMA(0, 1, At, B1); PG8_BAR; PG8_SCHED;
;             if constexpr (!HALFM) PG8_LDA(At, 0, 1); PG8_STAGE(PG8_SB(0, 0), b2, voffB); PG8_STAGE(PG8_SB(0, 1), b2 + hstep, voffB); if constexpr (GATHER) PG8_STAGE_G(PG8_SA(0, 0), kb2, s0); else PG8_STAGE(PG8_SA(0, 0), a2, voffA);
;             PG8_WAIT_V(8); PG8_WAIT_L(0); PG8_BAR; if constexpr (!HALFM) { PG8_MMA(1, 0, At, B0); PG8_MMA(1, 1, At, B1); } PG8_BAR; PG8_SCHED;
.Lup_unit_nobar:
.LBB0_1716:
	s_add_i32 s72, 0, 0x10000
	v_add_u32_e32 v161, s72, v170
	ds_read_b128 v[136:139], v161
	ds_read_b128 v[140:143], v161 offset:1024
	ds_read_b128 v[144:147], v161 offset:2048
	ds_read_b128 v[182:185], v161 offset:3072
	s_add_i32 s73, 0, 0x14000
	v_add_u32_e32 v161, s73, v170
	ds_read_b128 v[186:189], v161
	ds_read_b128 v[190:193], v161 offset:1024
	ds_read_b128 v[194:197], v161 offset:2048
	ds_read_b128 v[198:201], v161 offset:3072
	s_add_u32 s20, s36, s14
	s_addc_u32 s21, s82, s15
	s_add_u32 s24, s14, 0x100
	s_addc_u32 s25, s15, 0
	s_cmpk_eq_i32 s14, 0x700
	s_cselect_b64 vcc, -1, 0
	s_and_b64 s[4:5], vcc, exec
	s_cselect_b32 s5, s41, s21
	s_cselect_b32 s4, s40, s20
	s_cselect_b32 s20, 0, s24
	s_add_i32 s21, 0, 0x10000
	s_add_i32 s33, 0, 0x14000
	v_cndmask_b32_e32 v2, v148, v163, vcc
	v_cndmask_b32_e32 v153, v152, v167, vcc
	v_cndmask_b32_e32 v160, v150, v166, vcc
	v_cndmask_b32_e32 v155, v154, v168, vcc
	v_lshl_add_u64 v[220:221], v[134:135], 0, s[14:15]
	s_add_i32 m0, s12, 0xc000
	ds_read_b128 v[202:205], v177
	ds_read_b128 v[208:211], v177 offset:1024
	ds_read_b128 v[224:227], v177 offset:2048
	ds_read_b128 v[228:231], v177 offset:3072
	ds_read_b128 v[232:235], v177 offset:4096
	ds_read_b128 v[236:239], v177 offset:5120
	ds_read_b128 v[240:243], v177 offset:6144
	ds_read_b128 v[244:247], v177 offset:7168
	global_load_lds_dwordx4 v[220:221], off
	v_lshl_add_u64 v[220:221], v[132:133], 0, s[14:15]
	s_add_i32 m0, s12, 0xe000
	s_nop 0
	global_load_lds_dwordx4 v[220:221], off
	s_waitcnt vmcnt(8)
	s_waitcnt lgkmcnt(0)
	s_barrier
	s_setprio 1
	s_waitcnt lgkmcnt(0)
	v_mfma_f32_16x16x32_bf16 v[128:131], v[136:139], v[202:205], v[128:131]
	v_mfma_f32_16x16x32_bf16 v[124:127], v[144:147], v[202:205], v[124:127]
	v_mfma_f32_16x16x32_bf16 v[120:123], v[136:139], v[224:227], v[120:123]
	v_mfma_f32_16x16x32_bf16 v[116:119], v[144:147], v[224:227], v[116:119]
	v_mfma_f32_16x16x32_bf16 v[112:115], v[136:139], v[232:235], v[112:115]
	v_mfma_f32_16x16x32_bf16 v[108:111], v[144:147], v[232:235], v[108:111]
	v_mfma_f32_16x16x32_bf16 v[104:107], v[136:139], v[240:243], v[104:107]
	v_mfma_f32_16x16x32_bf16 v[100:103], v[144:147], v[240:243], v[100:103]
	v_mfma_f32_16x16x32_bf16 v[128:131], v[140:143], v[208:211], v[128:131]
	v_mfma_f32_16x16x32_bf16 v[124:127], v[182:185], v[208:211], v[124:127]
	v_mfma_f32_16x16x32_bf16 v[120:123], v[140:143], v[228:231], v[120:123]
	v_mfma_f32_16x16x32_bf16 v[116:119], v[182:185], v[228:231], v[116:119]
	v_mfma_f32_16x16x32_bf16 v[112:115], v[140:143], v[236:239], v[112:115]
	v_mfma_f32_16x16x32_bf16 v[108:111], v[182:185], v[236:239], v[108:111]
	v_mfma_f32_16x16x32_bf16 v[104:107], v[140:143], v[244:247], v[104:107]
	v_mfma_f32_16x16x32_bf16 v[100:103], v[182:185], v[244:247], v[100:103]
	s_setprio 0
	s_setprio 1
	v_mfma_f32_16x16x32_bf16 v[96:99], v[186:189], v[202:205], v[96:99]
	v_mfma_f32_16x16x32_bf16 v[92:95], v[194:197], v[202:205], v[92:95]
	v_mfma_f32_16x16x32_bf16 v[88:91], v[186:189], v[224:227], v[88:91]
	v_mfma_f32_16x16x32_bf16 v[84:87], v[194:197], v[224:227], v[84:87]
	v_mfma_f32_16x16x32_bf16 v[80:83], v[186:189], v[232:235], v[80:83]
	v_mfma_f32_16x16x32_bf16 v[76:79], v[194:197], v[232:235], v[76:79]
	v_mfma_f32_16x16x32_bf16 v[72:75], v[186:189], v[240:243], v[72:75]
	v_mfma_f32_16x16x32_bf16 v[68:71], v[194:197], v[240:243], v[68:71]
	v_mfma_f32_16x16x32_bf16 v[96:99], v[190:193], v[208:211], v[96:99]
	v_mfma_f32_16x16x32_bf16 v[92:95], v[198:201], v[208:211], v[92:95]
	v_mfma_f32_16x16x32_bf16 v[88:91], v[190:193], v[228:231], v[88:91]
	v_mfma_f32_16x16x32_bf16 v[84:87], v[198:201], v[228:231], v[84:87]
	v_mfma_f32_16x16x32_bf16 v[80:83], v[190:193], v[236:239], v[80:83]
	v_mfma_f32_16x16x32_bf16 v[76:79], v[198:201], v[236:239], v[76:79]
	v_mfma_f32_16x16x32_bf16 v[72:75], v[190:193], v[244:247], v[72:75]
	v_mfma_f32_16x16x32_bf16 v[68:71], v[198:201], v[244:247], v[68:71]
	s_setprio 0
	s_barrier
	s_add_i32 s14, s21, s8
	v_lshl_add_u64 v[220:221], s[4:5], 0, v[156:157]
	s_mov_b32 m0, s14
	ds_read_b128 v[202:205], v177 offset:16384
	ds_read_b128 v[208:211], v177 offset:17408
	ds_read_b128 v[224:227], v177 offset:18432
	ds_read_b128 v[228:231], v177 offset:19456
	ds_read_b128 v[232:235], v177 offset:20480
	ds_read_b128 v[236:239], v177 offset:21504
	ds_read_b128 v[240:243], v177 offset:22528
	ds_read_b128 v[244:247], v177 offset:23552
	global_load_lds_dwordx4 v[220:221], off
	s_add_i32 m0, s14, 0x2000
	s_add_u32 s14, s4, 0x40000
	v_lshl_add_u64 v[216:217], s[4:5], 0, v[158:159]
	s_addc_u32 s15, s5, 0
	s_add_i32 s21, s33, s8
	global_load_lds_dwordx4 v[216:217], off
	v_lshl_add_u64 v[218:219], s[14:15], 0, v[156:157]
	s_mov_b32 m0, s21
	v_mov_b32_e32 v161, v3
	global_load_lds_dwordx4 v[218:219], off
	s_add_i32 m0, s21, 0x2000
	v_lshl_add_u64 v[218:219], s[14:15], 0, v[158:159]
	s_add_u32 s14, s78, s20
	global_load_lds_dwordx4 v[218:219], off
	s_addc_u32 s15, s79, 0
	s_mov_b32 m0, s12
	v_lshl_add_u64 v[218:219], s[14:15], 0, v[2:3]
	global_load_lds_dwordx4 v2, s[14:15]
	s_mov_b32 m0, s13
	s_nop 0
	global_load_lds_dwordx4 v160, s[14:15]
	s_waitcnt vmcnt(8)
	s_waitcnt lgkmcnt(0)
	v_lshl_add_u64 v[160:161], s[14:15], 0, v[160:161]
	s_barrier
; #define PG8_STAGE(bufoff, gbase, voff) do { _Pragma("unroll") for (int _i = 0; _i < 2; ++_i) \
;         __builtin_amdgcn_global_load_lds((const unsigned*)((const char*)(gbase) + (voff)[_i]), (PG8_LAS unsigned*)(lds + (bufoff) + ldsw + _i * 8192), 16, 0, 0); } while (0)
; #define PG8_STAGE_G(bufoff, kb, g) do { _Pragma("unroll") for (int _i = 0; _i < 2; ++_i) \
;         __builtin_amdgcn_global_load_lds((const unsigned*)(gA + (size_t)(kb) + (g)[_i]), (PG8_LAS unsigned*)(lds + (bufoff) + ldsw + _i * 8192), 16, 0, 0); } while (0)
; #define PG8_LDA(dst, b, h) do { _Pragma("unroll") for (int m = 0; m < 4; ++m) _Pragma("unroll") for (int k = 0; k < 2; ++k) dst[m][k] = *(const PG8_LAS bf16x8*)(lds + PG8_SA(b, h) + aoff + m * 2048 + k * 1024); } while (0)
; #define PG8_LDB(dst, b, h) do { _Pragma("unroll") for (int n = 0; n < 2; ++n) _Pragma("unroll") for (int k = 0; k < 2; ++k) dst[n][k] = *(const PG8_LAS bf16x8*)(lds + PG8_SB(b, h) + boff + n * 2048 + k * 1024); } while (0)
; #define PG8_MMA(ai, bj, At, Bt) do { __builtin_amdgcn_s_setprio(1); _Pragma("unroll") for (int m = 0; m < 4; ++m) _Pragma("unroll") for (int n = 0; n < 2; ++n) _Pragma("unroll") for (int k = 0; k < 2; ++k) \
;         acc[ai][bj][m][n] = __builtin_amdgcn_mfma_f32_16x16x32_bf16(Bt[n][k], At[m][k], acc[ai][bj][m][n], 0, 0, 0); __builtin_amdgcn_s_setprio(0); } while (0)
; #define PG8_WAIT_V(n) asm volatile("s_waitcnt vmcnt(" #n ")" ::: "memory")
; #define PG8_WAIT_L(n) asm volatile("s_waitcnt lgkmcnt(" #n ")" ::: "memory")
; #define PG8_BAR __builtin_amdgcn_s_barrier()
; #define PG8_SCHED __builtin_amdgcn_sched_barrier(0)
; template <class Epi, class Sched, bool ALIGN_EPI = false, bool SP2 = false, bool GATHER = false, bool HALFM = false>
; __device__ __forceinline__ void gemm_phase(PG8_LAS unsigned char* lds, const int Kdim, const Sched& S, const Epi& E) {
;     ...
;             PG8_WAIT_V(8); PG8_WAIT_L(0); PG8_BAR; if constexpr (!HALFM) { PG8_MMA(1, 0, At, B0); PG8_MMA(1, 1, At, B1); } PG8_BAR; PG8_SCHED;
;             PG8_LDB(B0, 1, 0); PG8_LDB(B1, 1, 1); PG8_SCHED; PG8_LDA(At, 1, 0); if constexpr (GATHER) PG8_STAGE_G(PG8_SA(0, 1), kb2, s1); else PG8_STAGE(PG8_SA(0, 1), a2 + hstep, voffA);
;             PG8_WAIT_V(8); PG8_WAIT_L(0); PG8_BAR; PG8_MMA(0, 0, At, B0); PG8_MMA(0, 1, At, B1); PG8_BAR; PG8_SCHED;
	s_setprio 1
	s_waitcnt lgkmcnt(0)
	v_mfma_f32_16x16x32_bf16 v[64:67], v[136:139], v[202:205], v[64:67]
	v_mfma_f32_16x16x32_bf16 v[60:63], v[144:147], v[202:205], v[60:63]
	v_mfma_f32_16x16x32_bf16 v[56:59], v[136:139], v[224:227], v[56:59]
	v_mfma_f32_16x16x32_bf16 v[52:55], v[144:147], v[224:227], v[52:55]
	v_mfma_f32_16x16x32_bf16 v[48:51], v[136:139], v[232:235], v[48:51]
	v_mfma_f32_16x16x32_bf16 v[44:47], v[144:147], v[232:235], v[44:47]
	v_mfma_f32_16x16x32_bf16 v[40:43], v[136:139], v[240:243], v[40:43]
	v_mfma_f32_16x16x32_bf16 v[36:39], v[144:147], v[240:243], v[36:39]
	v_mfma_f32_16x16x32_bf16 v[64:67], v[140:143], v[208:211], v[64:67]
	v_mfma_f32_16x16x32_bf16 v[60:63], v[182:185], v[208:211], v[60:63]
	v_mfma_f32_16x16x32_bf16 v[56:59], v[140:143], v[228:231], v[56:59]
	v_mfma_f32_16x16x32_bf16 v[52:55], v[182:185], v[228:231], v[52:55]
	v_mfma_f32_16x16x32_bf16 v[48:51], v[140:143], v[236:239], v[48:51]
	v_mfma_f32_16x16x32_bf16 v[44:47], v[182:185], v[236:239], v[44:47]
	v_mfma_f32_16x16x32_bf16 v[40:43], v[140:143], v[244:247], v[40:43]
	v_mfma_f32_16x16x32_bf16 v[36:39], v[182:185], v[244:247], v[36:39]
	s_setprio 0
	s_setprio 1
	v_mfma_f32_16x16x32_bf16 v[32:35], v[186:189], v[202:205], v[32:35]
	v_mfma_f32_16x16x32_bf16 v[28:31], v[194:197], v[202:205], v[28:31]
	v_mfma_f32_16x16x32_bf16 v[24:27], v[186:189], v[224:227], v[24:27]
	v_mfma_f32_16x16x32_bf16 v[20:23], v[194:197], v[224:227], v[20:23]
	v_mfma_f32_16x16x32_bf16 v[16:19], v[186:189], v[232:235], v[16:19]
	v_mfma_f32_16x16x32_bf16 v[12:15], v[194:197], v[232:235], v[12:15]
	v_mfma_f32_16x16x32_bf16 v[8:11], v[186:189], v[240:243], v[8:11]
	v_mfma_f32_16x16x32_bf16 v[4:7], v[194:197], v[240:243], v[4:7]
	v_mfma_f32_16x16x32_bf16 v[32:35], v[190:193], v[208:211], v[32:35]
	v_mfma_f32_16x16x32_bf16 v[28:31], v[198:201], v[208:211], v[28:31]
	v_mfma_f32_16x16x32_bf16 v[24:27], v[190:193], v[228:231], v[24:27]
	v_mfma_f32_16x16x32_bf16 v[20:23], v[198:201], v[228:231], v[20:23]
	v_mfma_f32_16x16x32_bf16 v[16:19], v[190:193], v[236:239], v[16:19]
	v_mfma_f32_16x16x32_bf16 v[12:15], v[198:201], v[236:239], v[12:15]
	v_mfma_f32_16x16x32_bf16 v[8:11], v[190:193], v[244:247], v[8:11]
	v_mfma_f32_16x16x32_bf16 v[4:7], v[198:201], v[244:247], v[4:7]
	s_setprio 0
	s_barrier
	s_add_i32 s20, 0, 0x18000
	v_add_u32_e32 v2, s20, v170
	s_add_i32 s21, 0, 0x1c000
	ds_read_b128 v[136:139], v2
	ds_read_b128 v[140:143], v2 offset:1024
	ds_read_b128 v[144:147], v2 offset:2048
	ds_read_b128 v[182:185], v2 offset:3072
	v_add_u32_e32 v2, s21, v170
	ds_read_b128 v[186:189], v2
	ds_read_b128 v[190:193], v2 offset:1024
	ds_read_b128 v[194:197], v2 offset:2048
	ds_read_b128 v[198:201], v2 offset:3072
	s_mov_b32 m0, s22
	ds_read_b128 v[202:205], v177 offset:32768
	ds_read_b128 v[208:211], v177 offset:33792
	ds_read_b128 v[224:227], v177 offset:34816
	ds_read_b128 v[228:231], v177 offset:35840
	ds_read_b128 v[232:235], v177 offset:36864
	ds_read_b128 v[236:239], v177 offset:37888
	ds_read_b128 v[240:243], v177 offset:38912
	ds_read_b128 v[244:247], v177 offset:39936
	global_load_lds_dwordx4 v153, s[14:15]
	s_mov_b32 m0, s23
	s_nop 0
	global_load_lds_dwordx4 v155, s[14:15]
	s_waitcnt vmcnt(8)
	s_waitcnt lgkmcnt(0)
	s_barrier
	s_setprio 1
	s_waitcnt lgkmcnt(0)
	v_mfma_f32_16x16x32_bf16 v[128:131], v[136:139], v[202:205], v[128:131]
	v_mfma_f32_16x16x32_bf16 v[124:127], v[144:147], v[202:205], v[124:127]
	v_mfma_f32_16x16x32_bf16 v[120:123], v[136:139], v[224:227], v[120:123]
	v_mfma_f32_16x16x32_bf16 v[116:119], v[144:147], v[224:227], v[116:119]
	v_mfma_f32_16x16x32_bf16 v[112:115], v[136:139], v[232:235], v[112:115]
	v_mfma_f32_16x16x32_bf16 v[108:111], v[144:147], v[232:235], v[108:111]
	v_mfma_f32_16x16x32_bf16 v[104:107], v[136:139], v[240:243], v[104:107]
	v_mfma_f32_16x16x32_bf16 v[100:103], v[144:147], v[240:243], v[100:103]
	v_mfma_f32_16x16x32_bf16 v[128:131], v[140:143], v[208:211], v[128:131]
	v_mfma_f32_16x16x32_bf16 v[124:127], v[182:185], v[208:211], v[124:127]
	v_mfma_f32_16x16x32_bf16 v[120:123], v[140:143], v[228:231], v[120:123]
	v_mfma_f32_16x16x32_bf16 v[116:119], v[182:185], v[228:231], v[116:119]
	v_mfma_f32_16x16x32_bf16 v[112:115], v[140:143], v[236:239], v[112:115]
	v_mfma_f32_16x16x32_bf16 v[108:111], v[182:185], v[236:239], v[108:111]
	v_mfma_f32_16x16x32_bf16 v[104:107], v[140:143], v[244:247], v[104:107]
	v_mfma_f32_16x16x32_bf16 v[100:103], v[182:185], v[244:247], v[100:103]
	s_setprio 0
	s_setprio 1
	v_mfma_f32_16x16x32_bf16 v[96:99], v[186:189], v[202:205], v[96:99]
	v_mfma_f32_16x16x32_bf16 v[92:95], v[194:197], v[202:205], v[92:95]
	v_mfma_f32_16x16x32_bf16 v[88:91], v[186:189], v[224:227], v[88:91]
	v_mfma_f32_16x16x32_bf16 v[84:87], v[194:197], v[224:227], v[84:87]
	v_mfma_f32_16x16x32_bf16 v[80:83], v[186:189], v[232:235], v[80:83]
	v_mfma_f32_16x16x32_bf16 v[76:79], v[194:197], v[232:235], v[76:79]
	v_mfma_f32_16x16x32_bf16 v[72:75], v[186:189], v[240:243], v[72:75]
	v_mfma_f32_16x16x32_bf16 v[68:71], v[194:197], v[240:243], v[68:71]
	v_mfma_f32_16x16x32_bf16 v[96:99], v[190:193], v[208:211], v[96:99]
	v_mfma_f32_16x16x32_bf16 v[92:95], v[198:201], v[208:211], v[92:95]
	v_mfma_f32_16x16x32_bf16 v[88:91], v[190:193], v[228:231], v[88:91]
	v_mfma_f32_16x16x32_bf16 v[84:87], v[198:201], v[228:231], v[84:87]
	v_mfma_f32_16x16x32_bf16 v[80:83], v[190:193], v[236:239], v[80:83]
	v_mfma_f32_16x16x32_bf16 v[76:79], v[198:201], v[236:239], v[76:79]
	v_mfma_f32_16x16x32_bf16 v[72:75], v[190:193], v[244:247], v[72:75]
	v_mfma_f32_16x16x32_bf16 v[68:71], v[198:201], v[244:247], v[68:71]
	s_setprio 0
	s_barrier
; #define PG8_STAGE(bufoff, gbase, voff) do { _Pragma("unroll") for (int _i = 0; _i < 2; ++_i) \
;         __builtin_amdgcn_global_load_lds((const unsigned*)((const char*)(gbase) + (voff)[_i]), (PG8_LAS unsigned*)(lds + (bufoff) + ldsw + _i * 8192), 16, 0, 0); } while (0)
; #define PG8_STAGE_G(bufoff, kb, g) do { _Pragma("unroll") for (int _i = 0; _i < 2; ++_i) \
;         __builtin_amdgcn_global_load_lds((const unsigned*)(gA + (size_t)(kb) + (g)[_i]), (PG8_LAS unsigned*)(lds + (bufoff) + ldsw + _i * 8192), 16, 0, 0); } while (0)
; #define PG8_LDA(dst, b, h) do { _Pragma("unroll") for (int m = 0; m < 4; ++m) _Pragma("unroll") for (int k = 0; k < 2; ++k) dst[m][k] = *(const PG8_LAS bf16x8*)(lds + PG8_SA(b, h) + aoff + m * 2048 + k * 1024); } while (0)
; #define PG8_MMA(ai, bj, At, Bt) do { __builtin_amdgcn_s_setprio(1); _Pragma("unroll") for (int m = 0; m < 4; ++m) _Pragma("unroll") for (int n = 0; n < 2; ++n) _Pragma("unroll") for (int k = 0; k < 2; ++k) \
;         acc[ai][bj][m][n] = __builtin_amdgcn_mfma_f32_16x16x32_bf16(Bt[n][k], At[m][k], acc[ai][bj][m][n], 0, 0, 0); __builtin_amdgcn_s_setprio(0); } while (0)
; #define PG8_WAIT_V(n) asm volatile("s_waitcnt vmcnt(" #n ")" ::: "memory")
; #define PG8_WAIT_L(n) asm volatile("s_waitcnt lgkmcnt(" #n ")" ::: "memory")
; #define PG8_BAR __builtin_amdgcn_s_barrier()
; #define PG8_SCHED __builtin_amdgcn_sched_barrier(0)
; template <class Epi, class Sched, bool ALIGN_EPI = false, bool SP2 = false, bool GATHER = false, bool HALFM = false>
; __device__ __forceinline__ void gemm_phase(PG8_LAS unsigned char* lds, const int Kdim, const Sched& S, const Epi& E) {
;     ...
;             if constexpr (!HALFM) PG8_LDA(At, 1, 1); PG8_STAGE(PG8_SB(1, 0), b3, voffB); PG8_STAGE(PG8_SB(1, 1), b3 + hstep, voffB); if constexpr (GATHER) PG8_STAGE_G(PG8_SA(1, 0), kb2 + kstep, s0); else PG8_STAGE(PG8_SA(1, 0), a3, voffA);
;             PG8_WAIT_V(8); PG8_WAIT_L(0); PG8_BAR; if constexpr (!HALFM) { PG8_MMA(1, 0, At, B0); PG8_MMA(1, 1, At, B1); } PG8_BAR; PG8_SCHED;
	s_add_i32 s14, s20, s8
	v_lshl_add_u64 v[220:221], v[220:221], 0, s[34:35]
	s_mov_b32 m0, s14
	ds_read_b128 v[202:205], v177 offset:49152
	ds_read_b128 v[208:211], v177 offset:50176
	ds_read_b128 v[224:227], v177 offset:51200
	ds_read_b128 v[228:231], v177 offset:52224
	ds_read_b128 v[232:235], v177 offset:53248
	ds_read_b128 v[236:239], v177 offset:54272
	ds_read_b128 v[240:243], v177 offset:55296
	ds_read_b128 v[244:247], v177 offset:56320
	global_load_lds_dwordx4 v[220:221], off
	s_add_i32 m0, s14, 0x2000
	s_add_u32 s4, s4, 0x40080
	v_lshl_add_u64 v[216:217], v[216:217], 0, s[34:35]
	s_addc_u32 s5, s5, 0
	s_add_i32 s14, s21, s8
	global_load_lds_dwordx4 v[216:217], off
	v_lshl_add_u64 v[216:217], s[4:5], 0, v[156:157]
	s_mov_b32 m0, s14
	v_lshl_add_u64 v[160:161], v[160:161], 0, s[34:35]
	global_load_lds_dwordx4 v[216:217], off
	v_lshl_add_u64 v[216:217], s[4:5], 0, v[158:159]
	s_add_i32 m0, s14, 0x2000
	s_nop 0
	global_load_lds_dwordx4 v[216:217], off
	v_lshl_add_u64 v[216:217], v[218:219], 0, s[34:35]
	s_mov_b32 m0, s50
	s_nop 0
	global_load_lds_dwordx4 v[216:217], off
	s_mov_b32 m0, s51
	s_nop 0
	global_load_lds_dwordx4 v[160:161], off
	s_waitcnt vmcnt(8)
	s_waitcnt lgkmcnt(0)
	s_barrier
	s_setprio 1
	s_waitcnt lgkmcnt(0)
	v_mfma_f32_16x16x32_bf16 v[64:67], v[136:139], v[202:205], v[64:67]
	v_mfma_f32_16x16x32_bf16 v[60:63], v[144:147], v[202:205], v[60:63]
	v_mfma_f32_16x16x32_bf16 v[56:59], v[136:139], v[224:227], v[56:59]
	v_mfma_f32_16x16x32_bf16 v[52:55], v[144:147], v[224:227], v[52:55]
	v_mfma_f32_16x16x32_bf16 v[48:51], v[136:139], v[232:235], v[48:51]
	v_mfma_f32_16x16x32_bf16 v[44:47], v[144:147], v[232:235], v[44:47]
	v_mfma_f32_16x16x32_bf16 v[40:43], v[136:139], v[240:243], v[40:43]
	v_mfma_f32_16x16x32_bf16 v[36:39], v[144:147], v[240:243], v[36:39]
	v_mfma_f32_16x16x32_bf16 v[64:67], v[140:143], v[208:211], v[64:67]
	v_mfma_f32_16x16x32_bf16 v[60:63], v[182:185], v[208:211], v[60:63]
	v_mfma_f32_16x16x32_bf16 v[56:59], v[140:143], v[228:231], v[56:59]
	v_mfma_f32_16x16x32_bf16 v[52:55], v[182:185], v[228:231], v[52:55]
	v_mfma_f32_16x16x32_bf16 v[48:51], v[140:143], v[236:239], v[48:51]
	v_mfma_f32_16x16x32_bf16 v[44:47], v[182:185], v[236:239], v[44:47]
	v_mfma_f32_16x16x32_bf16 v[40:43], v[140:143], v[244:247], v[40:43]
	v_mfma_f32_16x16x32_bf16 v[36:39], v[182:185], v[244:247], v[36:39]
	s_setprio 0
	s_setprio 1
	v_mfma_f32_16x16x32_bf16 v[32:35], v[186:189], v[202:205], v[32:35]
	v_mfma_f32_16x16x32_bf16 v[28:31], v[194:197], v[202:205], v[28:31]
	v_mfma_f32_16x16x32_bf16 v[24:27], v[186:189], v[224:227], v[24:27]
	v_mfma_f32_16x16x32_bf16 v[20:23], v[194:197], v[224:227], v[20:23]
	v_mfma_f32_16x16x32_bf16 v[16:19], v[186:189], v[232:235], v[16:19]
	v_mfma_f32_16x16x32_bf16 v[12:15], v[194:197], v[232:235], v[12:15]
	v_mfma_f32_16x16x32_bf16 v[8:11], v[186:189], v[240:243], v[8:11]
	v_mfma_f32_16x16x32_bf16 v[4:7], v[194:197], v[240:243], v[4:7]
	v_mfma_f32_16x16x32_bf16 v[32:35], v[190:193], v[208:211], v[32:35]
	v_mfma_f32_16x16x32_bf16 v[28:31], v[198:201], v[208:211], v[28:31]
	v_mfma_f32_16x16x32_bf16 v[24:27], v[190:193], v[228:231], v[24:27]
	v_mfma_f32_16x16x32_bf16 v[20:23], v[198:201], v[228:231], v[20:23]
	v_mfma_f32_16x16x32_bf16 v[16:19], v[190:193], v[236:239], v[16:19]
	v_mfma_f32_16x16x32_bf16 v[12:15], v[198:201], v[236:239], v[12:15]
	v_mfma_f32_16x16x32_bf16 v[8:11], v[190:193], v[244:247], v[8:11]
	v_mfma_f32_16x16x32_bf16 v[4:7], v[198:201], v[244:247], v[4:7]
	s_setprio 0
	s_barrier
	s_add_i32 s83, s83, 2
	s_cmp_gt_u32 s83, 13
	s_mov_b64 s[14:15], s[24:25]
	s_cbranch_scc0 .LBB0_1716
	s_and_b64 vcc, exec, s[6:7]
	s_cbranch_vccz .LBB0_1719
	s_barrier

; #define PG8_STAGE(bufoff, gbase, voff) do { _Pragma("unroll") for (int _i = 0; _i < 2; ++_i) \
;         __builtin_amdgcn_global_load_lds((const unsigned*)((const char*)(gbase) + (voff)[_i]), (PG8_LAS unsigned*)(lds + (bufoff) + ldsw + _i * 8192), 16, 0, 0); } while (0)
; #define PG8_STAGE_G(bufoff, kb, g) do { _Pragma("unroll") for (int _i = 0; _i < 2; ++_i) \
;         __builtin_amdgcn_global_load_lds((const unsigned*)(gA + (size_t)(kb) + (g)[_i]), (PG8_LAS unsigned*)(lds + (bufoff) + ldsw + _i * 8192), 16, 0, 0); } while (0)
; #define PG8_WAIT_V(n) asm volatile("s_waitcnt vmcnt(" #n ")" ::: "memory")
; #define PG8_WAIT_L(n) asm volatile("s_waitcnt lgkmcnt(" #n ")" ::: "memory")
; #define PG8_BAR __builtin_amdgcn_s_barrier()
; template <class Epi, class Sched, bool ALIGN_EPI = false, bool SP2 = false, bool GATHER = false, bool HALFM = false>
; __device__ __forceinline__ void gemm_phase(PG8_LAS unsigned char* lds, const int Kdim, const Sched& S, const Epi& E) {
;     ...
;             const bool last = (t == nt - 2);
;             const char* a1 = cA + (size_t)(t + 1) * kstep;
;             const char* a2 = last ? nA : cA + (size_t)(t + 2) * kstep; const char* b2 = last ? nB : cB + (size_t)(t + 2) * kstep;
;             const char* a3 = a2 + kstep; const char* b3 = b2 + kstep;
;             if (last && has_next) S.a_ready(nxt);
;             unsigned s0[2] = {0u, 0u}, s1[2] = {0u, 0u}; size_t kb2 = 0;
;             if constexpr (GATHER) { kb2 = last ? (size_t)0 : (size_t)(t + 2) * kstep;
; #pragma unroll
;                 for (int i = 0; i < 2; ++i) { s0[i] = last ? gn[0][i] : gc[0][i]; s1[i] = last ? gn[1][i] : gc[1][i]; } }
;             if constexpr (SP2) {
;             PG8_LDB(B0, 0, 0); PG8_LDB(B1, 0, 1); PG8_SCHED; PG8_LDA(At, 0, 0); if constexpr (GATHER) PG8_STAGE_G(PG8_SA(1, 1), (size_t)(t + 1) * kstep, gc[1]); else PG8_STAGE(PG8_SA(1, 1), a1 + hstep, voffA);
;             PG8_WAIT_V(8); PG8_WAIT_L(0); PG8_BAR; PG8_MMA(0, 0, At, B0); PG8_MMA(0, 1, At, B1); PG8_BAR; PG8_SCHED;
;             if constexpr (!HALFM) PG8_LDA(At, 0, 1); PG8_STAGE(PG8_SB(0, 0), b2, voffB); PG8_STAGE(PG8_SB(0, 1), b2 + hstep, voffB); if constexpr (GATHER) PG8_STAGE_G(PG8_SA(0, 0), kb2, s0); else PG8_STAGE(PG8_SA(0, 0), a2, voffA);
;             PG8_WAIT_V(8); PG8_WAIT_L(0); PG8_BAR; if constexpr (!HALFM) { PG8_MMA(1, 0, At, B0); PG8_MMA(1, 1, At, B1); } PG8_BAR; PG8_SCHED;
.Ldn_unit_nobar:
.LBB0_1817:
	s_add_i32 s20, 0, 0x10000
	s_add_i32 s33, 0, 0x14000
	v_add_u32_e32 v112, s20, v160
	v_add_u32_e32 v158, s33, v160
	ds_read_b128 v[100:103], v112
	ds_read_b128 v[104:107], v112 offset:1024
	ds_read_b128 v[108:111], v112 offset:2048
	ds_read_b128 v[112:115], v112 offset:3072
	ds_read_b128 v[170:173], v158
	ds_read_b128 v[174:177], v158 offset:1024
	ds_read_b128 v[178:181], v158 offset:2048
	ds_read_b128 v[182:185], v158 offset:3072
	s_add_u32 s4, s44, 0xfffc0080
	s_addc_u32 s5, s45, -1
	s_cmp_eq_u32 s57, 12
	s_cselect_b32 s25, s17, s5
	s_cselect_b32 s24, s36, s4
	s_cselect_b32 s5, s53, s56
	s_cselect_b32 s4, s54, s55
	v_lshl_add_u64 v[158:159], s[44:45], 0, v[154:155]
	s_add_i32 m0, s7, 0xc000
	ds_read_b128 v[186:189], v169
	ds_read_b128 v[190:193], v169 offset:1024
	ds_read_b128 v[194:197], v169 offset:2048
	ds_read_b128 v[198:201], v169 offset:3072
	ds_read_b128 v[202:205], v169 offset:4096
	ds_read_b128 v[208:211], v169 offset:5120
	ds_read_b128 v[224:227], v169 offset:6144
	ds_read_b128 v[228:231], v169 offset:7168
	global_load_lds_dwordx4 v[158:159], off
	v_lshl_add_u64 v[158:159], s[44:45], 0, v[156:157]
	s_add_i32 m0, s7, 0xe000
	s_nop 0
	global_load_lds_dwordx4 v[158:159], off
	s_waitcnt vmcnt(8)
	s_waitcnt lgkmcnt(0)
	s_barrier
	s_setprio 1
	s_waitcnt lgkmcnt(0)
	v_mfma_f32_16x16x32_bf16 v[144:147], v[100:103], v[186:189], v[144:147]
	v_mfma_f32_16x16x32_bf16 v[140:143], v[108:111], v[186:189], v[140:143]
	v_mfma_f32_16x16x32_bf16 v[128:131], v[100:103], v[194:197], v[128:131]
	v_mfma_f32_16x16x32_bf16 v[124:127], v[108:111], v[194:197], v[124:127]
	v_mfma_f32_16x16x32_bf16 v[96:99], v[100:103], v[202:205], v[96:99]
	v_mfma_f32_16x16x32_bf16 v[92:95], v[108:111], v[202:205], v[92:95]
	v_mfma_f32_16x16x32_bf16 v[80:83], v[100:103], v[224:227], v[80:83]
	v_mfma_f32_16x16x32_bf16 v[76:79], v[108:111], v[224:227], v[76:79]
	v_mfma_f32_16x16x32_bf16 v[144:147], v[104:107], v[190:193], v[144:147]
	v_mfma_f32_16x16x32_bf16 v[140:143], v[112:115], v[190:193], v[140:143]
	v_mfma_f32_16x16x32_bf16 v[128:131], v[104:107], v[198:201], v[128:131]
	v_mfma_f32_16x16x32_bf16 v[124:127], v[112:115], v[198:201], v[124:127]
	v_mfma_f32_16x16x32_bf16 v[96:99], v[104:107], v[208:211], v[96:99]
	v_mfma_f32_16x16x32_bf16 v[92:95], v[112:115], v[208:211], v[92:95]
	v_mfma_f32_16x16x32_bf16 v[80:83], v[104:107], v[228:231], v[80:83]
	v_mfma_f32_16x16x32_bf16 v[76:79], v[112:115], v[228:231], v[76:79]
	s_setprio 0
	s_setprio 1
	v_mfma_f32_16x16x32_bf16 v[136:139], v[170:173], v[186:189], v[136:139]
	v_mfma_f32_16x16x32_bf16 v[132:135], v[178:181], v[186:189], v[132:135]
	v_mfma_f32_16x16x32_bf16 v[120:123], v[170:173], v[194:197], v[120:123]
	v_mfma_f32_16x16x32_bf16 v[116:119], v[178:181], v[194:197], v[116:119]
	v_mfma_f32_16x16x32_bf16 v[88:91], v[170:173], v[202:205], v[88:91]
	v_mfma_f32_16x16x32_bf16 v[84:87], v[178:181], v[202:205], v[84:87]
	v_mfma_f32_16x16x32_bf16 v[72:75], v[170:173], v[224:227], v[72:75]
	v_mfma_f32_16x16x32_bf16 v[68:71], v[178:181], v[224:227], v[68:71]
	v_mfma_f32_16x16x32_bf16 v[136:139], v[174:177], v[190:193], v[136:139]
	v_mfma_f32_16x16x32_bf16 v[132:135], v[182:185], v[190:193], v[132:135]
	v_mfma_f32_16x16x32_bf16 v[120:123], v[174:177], v[198:201], v[120:123]
	v_mfma_f32_16x16x32_bf16 v[116:119], v[182:185], v[198:201], v[116:119]
	v_mfma_f32_16x16x32_bf16 v[88:91], v[174:177], v[208:211], v[88:91]
	v_mfma_f32_16x16x32_bf16 v[84:87], v[182:185], v[208:211], v[84:87]
	v_mfma_f32_16x16x32_bf16 v[72:75], v[174:177], v[228:231], v[72:75]
	v_mfma_f32_16x16x32_bf16 v[68:71], v[182:185], v[228:231], v[68:71]
	s_setprio 0
	s_barrier
	s_add_i32 s20, s20, s13
	v_lshl_add_u64 v[158:159], s[4:5], 0, v[2:3]
	s_mov_b32 m0, s20
	ds_read_b128 v[186:189], v169 offset:16384
	ds_read_b128 v[190:193], v169 offset:17408
	ds_read_b128 v[194:197], v169 offset:18432
	ds_read_b128 v[198:201], v169 offset:19456
	ds_read_b128 v[202:205], v169 offset:20480
	ds_read_b128 v[208:211], v169 offset:21504
	ds_read_b128 v[224:227], v169 offset:22528
	ds_read_b128 v[228:231], v169 offset:23552
	global_load_lds_dwordx4 v[158:159], off
	s_add_i32 m0, s20, 0x2000
	s_add_u32 s20, s4, 0x40000
	v_lshl_add_u64 v[216:217], s[4:5], 0, v[148:149]
	s_addc_u32 s21, s5, 0
	s_add_i32 s33, s33, s13
	global_load_lds_dwordx4 v[216:217], off
	v_lshl_add_u64 v[218:219], s[20:21], 0, v[2:3]
	s_mov_b32 m0, s33
	v_lshl_add_u64 v[220:221], s[24:25], 0, v[150:151]
	global_load_lds_dwordx4 v[218:219], off
	v_lshl_add_u64 v[218:219], s[20:21], 0, v[148:149]
	s_add_i32 m0, s33, 0x2000
	s_nop 0
	global_load_lds_dwordx4 v[218:219], off
	v_lshl_add_u64 v[218:219], s[24:25], 0, v[152:153]
	s_mov_b32 m0, s7
	s_nop 0
	global_load_lds_dwordx4 v[218:219], off
	s_mov_b32 m0, s22
	s_nop 0
	global_load_lds_dwordx4 v[220:221], off
	s_waitcnt vmcnt(8)
	s_waitcnt lgkmcnt(0)
	s_barrier
; #define PG8_STAGE(bufoff, gbase, voff) do { _Pragma("unroll") for (int _i = 0; _i < 2; ++_i) \
;         __builtin_amdgcn_global_load_lds((const unsigned*)((const char*)(gbase) + (voff)[_i]), (PG8_LAS unsigned*)(lds + (bufoff) + ldsw + _i * 8192), 16, 0, 0); } while (0)
; #define PG8_STAGE_G(bufoff, kb, g) do { _Pragma("unroll") for (int _i = 0; _i < 2; ++_i) \
;         __builtin_amdgcn_global_load_lds((const unsigned*)(gA + (size_t)(kb) + (g)[_i]), (PG8_LAS unsigned*)(lds + (bufoff) + ldsw + _i * 8192), 16, 0, 0); } while (0)
; #define PG8_LDA(dst, b, h) do { _Pragma("unroll") for (int m = 0; m < 4; ++m) _Pragma("unroll") for (int k = 0; k < 2; ++k) dst[m][k] = *(const PG8_LAS bf16x8*)(lds + PG8_SA(b, h) + aoff + m * 2048 + k * 1024); } while (0)
; #define PG8_LDB(dst, b, h) do { _Pragma("unroll") for (int n = 0; n < 2; ++n) _Pragma("unroll") for (int k = 0; k < 2; ++k) dst[n][k] = *(const PG8_LAS bf16x8*)(lds + PG8_SB(b, h) + boff + n * 2048 + k * 1024); } while (0)
; #define PG8_MMA(ai, bj, At, Bt) do { __builtin_amdgcn_s_setprio(1); _Pragma("unroll") for (int m = 0; m < 4; ++m) _Pragma("unroll") for (int n = 0; n < 2; ++n) _Pragma("unroll") for (int k = 0; k < 2; ++k) \
;         acc[ai][bj][m][n] = __builtin_amdgcn_mfma_f32_16x16x32_bf16(Bt[n][k], At[m][k], acc[ai][bj][m][n], 0, 0, 0); __builtin_amdgcn_s_setprio(0); } while (0)
; #define PG8_WAIT_V(n) asm volatile("s_waitcnt vmcnt(" #n ")" ::: "memory")
; #define PG8_WAIT_L(n) asm volatile("s_waitcnt lgkmcnt(" #n ")" ::: "memory")
; #define PG8_BAR __builtin_amdgcn_s_barrier()
; #define PG8_SCHED __builtin_amdgcn_sched_barrier(0)
; template <class Epi, class Sched, bool ALIGN_EPI = false, bool SP2 = false, bool GATHER = false, bool HALFM = false>
; __device__ __forceinline__ void gemm_phase(PG8_LAS unsigned char* lds, const int Kdim, const Sched& S, const Epi& E) {
;     ...
;             PG8_WAIT_V(8); PG8_WAIT_L(0); PG8_BAR; if constexpr (!HALFM) { PG8_MMA(1, 0, At, B0); PG8_MMA(1, 1, At, B1); } PG8_BAR; PG8_SCHED;
;             PG8_LDB(B0, 1, 0); PG8_LDB(B1, 1, 1); PG8_SCHED; PG8_LDA(At, 1, 0); if constexpr (GATHER) PG8_STAGE_G(PG8_SA(0, 1), kb2, s1); else PG8_STAGE(PG8_SA(0, 1), a2 + hstep, voffA);
;             PG8_WAIT_V(8); PG8_WAIT_L(0); PG8_BAR; PG8_MMA(0, 0, At, B0); PG8_MMA(0, 1, At, B1); PG8_BAR; PG8_SCHED;
	s_setprio 1
	s_waitcnt lgkmcnt(0)
	v_mfma_f32_16x16x32_bf16 v[64:67], v[100:103], v[186:189], v[64:67]
	v_mfma_f32_16x16x32_bf16 v[60:63], v[108:111], v[186:189], v[60:63]
	v_mfma_f32_16x16x32_bf16 v[52:55], v[100:103], v[194:197], v[52:55]
	v_mfma_f32_16x16x32_bf16 v[44:47], v[108:111], v[194:197], v[44:47]
	v_mfma_f32_16x16x32_bf16 v[36:39], v[100:103], v[202:205], v[36:39]
	v_mfma_f32_16x16x32_bf16 v[28:31], v[108:111], v[202:205], v[28:31]
	v_mfma_f32_16x16x32_bf16 v[20:23], v[100:103], v[224:227], v[20:23]
	v_mfma_f32_16x16x32_bf16 v[12:15], v[108:111], v[224:227], v[12:15]
	v_mfma_f32_16x16x32_bf16 v[64:67], v[104:107], v[190:193], v[64:67]
	v_mfma_f32_16x16x32_bf16 v[60:63], v[112:115], v[190:193], v[60:63]
	v_mfma_f32_16x16x32_bf16 v[52:55], v[104:107], v[198:201], v[52:55]
	v_mfma_f32_16x16x32_bf16 v[44:47], v[112:115], v[198:201], v[44:47]
	v_mfma_f32_16x16x32_bf16 v[36:39], v[104:107], v[208:211], v[36:39]
	v_mfma_f32_16x16x32_bf16 v[28:31], v[112:115], v[208:211], v[28:31]
	v_mfma_f32_16x16x32_bf16 v[20:23], v[104:107], v[228:231], v[20:23]
	v_mfma_f32_16x16x32_bf16 v[12:15], v[112:115], v[228:231], v[12:15]
	s_setprio 0
	s_setprio 1
	v_mfma_f32_16x16x32_bf16 v[56:59], v[170:173], v[186:189], v[56:59]
	v_mfma_f32_16x16x32_bf16 v[48:51], v[178:181], v[186:189], v[48:51]
	v_mfma_f32_16x16x32_bf16 v[40:43], v[170:173], v[194:197], v[40:43]
	v_mfma_f32_16x16x32_bf16 v[32:35], v[178:181], v[194:197], v[32:35]
	v_mfma_f32_16x16x32_bf16 v[24:27], v[170:173], v[202:205], v[24:27]
	v_mfma_f32_16x16x32_bf16 v[16:19], v[178:181], v[202:205], v[16:19]
	v_mfma_f32_16x16x32_bf16 v[8:11], v[170:173], v[224:227], v[8:11]
	v_mfma_f32_16x16x32_bf16 v[4:7], v[178:181], v[224:227], v[4:7]
	v_mfma_f32_16x16x32_bf16 v[56:59], v[174:177], v[190:193], v[56:59]
	v_mfma_f32_16x16x32_bf16 v[48:51], v[182:185], v[190:193], v[48:51]
	v_mfma_f32_16x16x32_bf16 v[40:43], v[174:177], v[198:201], v[40:43]
	v_mfma_f32_16x16x32_bf16 v[32:35], v[182:185], v[198:201], v[32:35]
	v_mfma_f32_16x16x32_bf16 v[24:27], v[174:177], v[208:211], v[24:27]
	v_mfma_f32_16x16x32_bf16 v[16:19], v[182:185], v[208:211], v[16:19]
	v_mfma_f32_16x16x32_bf16 v[8:11], v[174:177], v[228:231], v[8:11]
	v_mfma_f32_16x16x32_bf16 v[4:7], v[182:185], v[228:231], v[4:7]
	s_setprio 0
	s_barrier
	s_add_i32 s33, 0, 0x18000
	s_add_i32 s76, 0, 0x1c000
	v_add_u32_e32 v112, s33, v160
	v_add_u32_e32 v182, s76, v160
	ds_read_b128 v[100:103], v112
	ds_read_b128 v[104:107], v112 offset:1024
	ds_read_b128 v[108:111], v112 offset:2048
	ds_read_b128 v[112:115], v112 offset:3072
	ds_read_b128 v[170:173], v182
	ds_read_b128 v[174:177], v182 offset:1024
	ds_read_b128 v[178:181], v182 offset:2048
	ds_read_b128 v[182:185], v182 offset:3072
	s_add_u32 s20, s24, 0x40000
	s_addc_u32 s21, s25, 0
	s_mov_b32 m0, s23
	v_lshl_add_u64 v[232:233], s[20:21], 0, v[152:153]
	ds_read_b128 v[186:189], v169 offset:32768
	ds_read_b128 v[190:193], v169 offset:33792
	ds_read_b128 v[194:197], v169 offset:34816
	ds_read_b128 v[198:201], v169 offset:35840
	ds_read_b128 v[202:205], v169 offset:36864
	ds_read_b128 v[208:211], v169 offset:37888
	ds_read_b128 v[224:227], v169 offset:38912
	ds_read_b128 v[228:231], v169 offset:39936
	global_load_lds_dwordx4 v[232:233], off
	v_lshl_add_u64 v[232:233], s[20:21], 0, v[150:151]
	s_mov_b32 m0, s26
	s_nop 0
	global_load_lds_dwordx4 v[232:233], off
	s_waitcnt vmcnt(8)
	s_waitcnt lgkmcnt(0)
	s_barrier
	s_setprio 1
	s_waitcnt lgkmcnt(0)
	v_mfma_f32_16x16x32_bf16 v[144:147], v[100:103], v[186:189], v[144:147]
	v_mfma_f32_16x16x32_bf16 v[140:143], v[108:111], v[186:189], v[140:143]
	v_mfma_f32_16x16x32_bf16 v[128:131], v[100:103], v[194:197], v[128:131]
	v_mfma_f32_16x16x32_bf16 v[124:127], v[108:111], v[194:197], v[124:127]
	v_mfma_f32_16x16x32_bf16 v[96:99], v[100:103], v[202:205], v[96:99]
	v_mfma_f32_16x16x32_bf16 v[92:95], v[108:111], v[202:205], v[92:95]
	v_mfma_f32_16x16x32_bf16 v[80:83], v[100:103], v[224:227], v[80:83]
	v_mfma_f32_16x16x32_bf16 v[76:79], v[108:111], v[224:227], v[76:79]
	v_mfma_f32_16x16x32_bf16 v[144:147], v[104:107], v[190:193], v[144:147]
	v_mfma_f32_16x16x32_bf16 v[140:143], v[112:115], v[190:193], v[140:143]
	v_mfma_f32_16x16x32_bf16 v[128:131], v[104:107], v[198:201], v[128:131]
	v_mfma_f32_16x16x32_bf16 v[124:127], v[112:115], v[198:201], v[124:127]
	v_mfma_f32_16x16x32_bf16 v[96:99], v[104:107], v[208:211], v[96:99]
	v_mfma_f32_16x16x32_bf16 v[92:95], v[112:115], v[208:211], v[92:95]
	v_mfma_f32_16x16x32_bf16 v[80:83], v[104:107], v[228:231], v[80:83]
	v_mfma_f32_16x16x32_bf16 v[76:79], v[112:115], v[228:231], v[76:79]
	s_setprio 0
	s_setprio 1
	v_mfma_f32_16x16x32_bf16 v[136:139], v[170:173], v[186:189], v[136:139]
	v_mfma_f32_16x16x32_bf16 v[132:135], v[178:181], v[186:189], v[132:135]
	v_mfma_f32_16x16x32_bf16 v[120:123], v[170:173], v[194:197], v[120:123]
	v_mfma_f32_16x16x32_bf16 v[116:119], v[178:181], v[194:197], v[116:119]
	v_mfma_f32_16x16x32_bf16 v[88:91], v[170:173], v[202:205], v[88:91]
	v_mfma_f32_16x16x32_bf16 v[84:87], v[178:181], v[202:205], v[84:87]
	v_mfma_f32_16x16x32_bf16 v[72:75], v[170:173], v[224:227], v[72:75]
	v_mfma_f32_16x16x32_bf16 v[68:71], v[178:181], v[224:227], v[68:71]
	v_mfma_f32_16x16x32_bf16 v[136:139], v[174:177], v[190:193], v[136:139]
	v_mfma_f32_16x16x32_bf16 v[132:135], v[182:185], v[190:193], v[132:135]
	v_mfma_f32_16x16x32_bf16 v[120:123], v[174:177], v[198:201], v[120:123]
	v_mfma_f32_16x16x32_bf16 v[116:119], v[182:185], v[198:201], v[116:119]
	v_mfma_f32_16x16x32_bf16 v[88:91], v[174:177], v[208:211], v[88:91]
	v_mfma_f32_16x16x32_bf16 v[84:87], v[182:185], v[208:211], v[84:87]
	v_mfma_f32_16x16x32_bf16 v[72:75], v[174:177], v[228:231], v[72:75]
	v_mfma_f32_16x16x32_bf16 v[68:71], v[182:185], v[228:231], v[68:71]
	s_setprio 0
	s_barrier
; #define PG8_STAGE(bufoff, gbase, voff) do { _Pragma("unroll") for (int _i = 0; _i < 2; ++_i) \
;         __builtin_amdgcn_global_load_lds((const unsigned*)((const char*)(gbase) + (voff)[_i]), (PG8_LAS unsigned*)(lds + (bufoff) + ldsw + _i * 8192), 16, 0, 0); } while (0)
; #define PG8_STAGE_G(bufoff, kb, g) do { _Pragma("unroll") for (int _i = 0; _i < 2; ++_i) \
;         __builtin_amdgcn_global_load_lds((const unsigned*)(gA + (size_t)(kb) + (g)[_i]), (PG8_LAS unsigned*)(lds + (bufoff) + ldsw + _i * 8192), 16, 0, 0); } while (0)
; #define PG8_LDA(dst, b, h) do { _Pragma("unroll") for (int m = 0; m < 4; ++m) _Pragma("unroll") for (int k = 0; k < 2; ++k) dst[m][k] = *(const PG8_LAS bf16x8*)(lds + PG8_SA(b, h) + aoff + m * 2048 + k * 1024); } while (0)
; #define PG8_MMA(ai, bj, At, Bt) do { __builtin_amdgcn_s_setprio(1); _Pragma("unroll") for (int m = 0; m < 4; ++m) _Pragma("unroll") for (int n = 0; n < 2; ++n) _Pragma("unroll") for (int k = 0; k < 2; ++k) \
;         acc[ai][bj][m][n] = __builtin_amdgcn_mfma_f32_16x16x32_bf16(Bt[n][k], At[m][k], acc[ai][bj][m][n], 0, 0, 0); __builtin_amdgcn_s_setprio(0); } while (0)
; #define PG8_WAIT_V(n) asm volatile("s_waitcnt vmcnt(" #n ")" ::: "memory")
; #define PG8_WAIT_L(n) asm volatile("s_waitcnt lgkmcnt(" #n ")" ::: "memory")
; #define PG8_BAR __builtin_amdgcn_s_barrier()
; #define PG8_SCHED __builtin_amdgcn_sched_barrier(0)
; template <class Epi, class Sched, bool ALIGN_EPI = false, bool SP2 = false, bool GATHER = false, bool HALFM = false>
; __device__ __forceinline__ void gemm_phase(PG8_LAS unsigned char* lds, const int Kdim, const Sched& S, const Epi& E) {
;     ...
;             if constexpr (!HALFM) PG8_LDA(At, 1, 1); PG8_STAGE(PG8_SB(1, 0), b3, voffB); PG8_STAGE(PG8_SB(1, 1), b3 + hstep, voffB); if constexpr (GATHER) PG8_STAGE_G(PG8_SA(1, 0), kb2 + kstep, s0); else PG8_STAGE(PG8_SA(1, 0), a3, voffA);
;             PG8_WAIT_V(8); PG8_WAIT_L(0); PG8_BAR; if constexpr (!HALFM) { PG8_MMA(1, 0, At, B0); PG8_MMA(1, 1, At, B1); } PG8_BAR; PG8_SCHED;
	s_add_i32 s20, s33, s13
	v_lshl_add_u64 v[158:159], v[158:159], 0, s[34:35]
	s_mov_b32 m0, s20
	ds_read_b128 v[186:189], v169 offset:49152
	ds_read_b128 v[190:193], v169 offset:50176
	ds_read_b128 v[194:197], v169 offset:51200
	ds_read_b128 v[198:201], v169 offset:52224
	ds_read_b128 v[202:205], v169 offset:53248
	ds_read_b128 v[208:211], v169 offset:54272
	ds_read_b128 v[224:227], v169 offset:55296
	ds_read_b128 v[228:231], v169 offset:56320
	global_load_lds_dwordx4 v[158:159], off
	s_add_i32 m0, s20, 0x2000
	s_add_u32 s4, s4, 0x40080
	v_lshl_add_u64 v[158:159], v[216:217], 0, s[34:35]
	s_addc_u32 s5, s5, 0
	s_add_i32 s20, s76, s13
	global_load_lds_dwordx4 v[158:159], off
	v_lshl_add_u64 v[158:159], s[4:5], 0, v[2:3]
	s_mov_b32 m0, s20
	s_nop 0
	global_load_lds_dwordx4 v[158:159], off
	v_lshl_add_u64 v[158:159], s[4:5], 0, v[148:149]
	s_add_i32 m0, s20, 0x2000
	s_nop 0
	global_load_lds_dwordx4 v[158:159], off
	v_lshl_add_u64 v[158:159], v[218:219], 0, s[34:35]
	s_mov_b32 m0, s46
	s_nop 0
	global_load_lds_dwordx4 v[158:159], off
	v_lshl_add_u64 v[158:159], v[220:221], 0, s[34:35]
	s_mov_b32 m0, s47
	s_nop 0
	global_load_lds_dwordx4 v[158:159], off
	s_waitcnt vmcnt(8)
	s_waitcnt lgkmcnt(0)
	s_barrier
	s_setprio 1
	s_waitcnt lgkmcnt(0)
	v_mfma_f32_16x16x32_bf16 v[64:67], v[100:103], v[186:189], v[64:67]
	v_mfma_f32_16x16x32_bf16 v[60:63], v[108:111], v[186:189], v[60:63]
	v_mfma_f32_16x16x32_bf16 v[52:55], v[100:103], v[194:197], v[52:55]
	v_mfma_f32_16x16x32_bf16 v[44:47], v[108:111], v[194:197], v[44:47]
	v_mfma_f32_16x16x32_bf16 v[36:39], v[100:103], v[202:205], v[36:39]
	v_mfma_f32_16x16x32_bf16 v[28:31], v[108:111], v[202:205], v[28:31]
	v_mfma_f32_16x16x32_bf16 v[20:23], v[100:103], v[224:227], v[20:23]
	v_mfma_f32_16x16x32_bf16 v[12:15], v[108:111], v[224:227], v[12:15]
	v_mfma_f32_16x16x32_bf16 v[64:67], v[104:107], v[190:193], v[64:67]
	v_mfma_f32_16x16x32_bf16 v[60:63], v[112:115], v[190:193], v[60:63]
	v_mfma_f32_16x16x32_bf16 v[52:55], v[104:107], v[198:201], v[52:55]
	v_mfma_f32_16x16x32_bf16 v[44:47], v[112:115], v[198:201], v[44:47]
	v_mfma_f32_16x16x32_bf16 v[36:39], v[104:107], v[208:211], v[36:39]
	v_mfma_f32_16x16x32_bf16 v[28:31], v[112:115], v[208:211], v[28:31]
	v_mfma_f32_16x16x32_bf16 v[20:23], v[104:107], v[228:231], v[20:23]
	v_mfma_f32_16x16x32_bf16 v[12:15], v[112:115], v[228:231], v[12:15]
	s_setprio 0
	s_setprio 1
	v_mfma_f32_16x16x32_bf16 v[56:59], v[170:173], v[186:189], v[56:59]
	v_mfma_f32_16x16x32_bf16 v[48:51], v[178:181], v[186:189], v[48:51]
	v_mfma_f32_16x16x32_bf16 v[40:43], v[170:173], v[194:197], v[40:43]
	v_mfma_f32_16x16x32_bf16 v[32:35], v[178:181], v[194:197], v[32:35]
	v_mfma_f32_16x16x32_bf16 v[24:27], v[170:173], v[202:205], v[24:27]
	v_mfma_f32_16x16x32_bf16 v[16:19], v[178:181], v[202:205], v[16:19]
	v_mfma_f32_16x16x32_bf16 v[8:11], v[170:173], v[224:227], v[8:11]
	v_mfma_f32_16x16x32_bf16 v[4:7], v[178:181], v[224:227], v[4:7]
	v_mfma_f32_16x16x32_bf16 v[56:59], v[174:177], v[190:193], v[56:59]
	v_mfma_f32_16x16x32_bf16 v[48:51], v[182:185], v[190:193], v[48:51]
	v_mfma_f32_16x16x32_bf16 v[40:43], v[174:177], v[198:201], v[40:43]
	v_mfma_f32_16x16x32_bf16 v[32:35], v[182:185], v[198:201], v[32:35]
	v_mfma_f32_16x16x32_bf16 v[24:27], v[174:177], v[208:211], v[24:27]
	v_mfma_f32_16x16x32_bf16 v[16:19], v[182:185], v[208:211], v[16:19]
	v_mfma_f32_16x16x32_bf16 v[8:11], v[174:177], v[228:231], v[8:11]
	v_mfma_f32_16x16x32_bf16 v[4:7], v[182:185], v[228:231], v[4:7]
	s_setprio 0
	s_barrier
	s_add_i32 s57, s57, 2
	s_add_u32 s44, s44, 0x100
	s_addc_u32 s45, s45, 0
	s_add_u32 s55, s55, 0x100
	s_addc_u32 s56, s56, 0
	s_cmp_gt_u32 s57, 13
	s_cbranch_scc0 .LBB0_1817
	s_and_b64 vcc, exec, s[14:15]
	s_cbranch_vccz .LBB0_1820
	s_barrier
